# speedup vs baseline: 1.0027x; 1.0027x over previous
.LBB2_62:
	s_and_b64 vcc, exec, s[0:1]
	s_cbranch_vccz .LBB2_78
	v_and_b32_e32 v62, 63, v0
	v_lshlrev_b32_e32 v63, 2, v0
	s_mov_b32 s0, 0x1ffffe00
	v_and_or_b32 v62, v63, s0, v62
	v_lshlrev_b32_e32 v60, 3, v62
	v_ashrrev_i32_e32 v61, 31, v60
	v_lshl_add_u64 v[60:61], v[60:61], 1, s[16:17]
	s_movk_i32 s0, 0x1000
	v_add_co_u32_e32 v62, vcc, s0, v60
	v_and_b32_e32 v98, 31, v0
	v_lshlrev_b32_e32 v98, 2, v98
	v_addc_co_u32_e32 v63, vcc, 0, v61, vcc
	global_load_dwordx4 v[64:67], v[60:61], off
	global_load_dwordx4 v[68:71], v[60:61], off offset:1024
	global_load_dwordx4 v[72:75], v[60:61], off offset:2048
	global_load_dwordx4 v[76:79], v[62:63], off
	global_load_dwordx4 v[80:83], v[62:63], off offset:1024
	global_load_dwordx4 v[84:87], v[62:63], off offset:2048
	global_load_dwordx4 v[88:91], v[60:61], off offset:3072
	global_load_dwordx4 v[92:95], v[62:63], off offset:3072
	global_load_dword v96, v98, s[18:19]
	global_load_dword v97, v98, s[18:19] offset:128
	v_lshrrev_b32_e32 v2, 3, v0
	v_bitop3_b32 v2, v2, v1, 15 bitop3:0x6c
	s_waitcnt lgkmcnt(0)
	v_ashrrev_i32_e32 v35, 31, v34
	v_lshlrev_b32_e32 v2, 4, v2
	v_lshlrev_b64 v[6:7], 7, v[34:35]
	v_lshl_or_b32 v2, v36, 9, v2
	ds_read_b128 v[2:5], v2
	v_lshl_add_u64 v[6:7], s[26:27], 0, v[6:7]
	v_lshlrev_b32_e32 v34, 1, v37
	v_mov_b32_e32 v35, 0
	v_add_u32_e32 v36, 0x100, v0
	v_lshl_add_u64 v[6:7], v[6:7], 0, v[34:35]
	s_waitcnt lgkmcnt(0)
	global_store_dwordx4 v[6:7], v[2:5], off sc1
	s_nop 1
	v_ashrrev_i32_e32 v2, 3, v36
	v_lshlrev_b32_e32 v3, 2, v2
	ds_read_b32 v6, v3 offset:40448
	v_bitop3_b32 v1, v2, v1, 15 bitop3:0x6c
	v_lshlrev_b32_e32 v1, 4, v1
	v_lshl_or_b32 v1, v2, 9, v1
	ds_read_b128 v[2:5], v1
	s_waitcnt lgkmcnt(1)
	v_ashrrev_i32_e32 v7, 31, v6
	v_lshlrev_b64 v[6:7], 7, v[6:7]
	v_lshl_add_u64 v[6:7], s[26:27], 0, v[6:7]
	v_lshl_add_u64 v[6:7], v[6:7], 0, v[34:35]
	s_waitcnt lgkmcnt(0)
	global_store_dwordx4 v[6:7], v[2:5], off sc1
	s_nop 1
	v_lshrrev_b32_e32 v1, 1, v0
	v_and_b32_e32 v37, 31, v0
	v_and_b32_e32 v39, 32, v1
	v_bfe_u32 v38, v0, 5, 1
	v_or_b32_e32 v6, v39, v37
	v_bitop3_b32 v1, v38, v0, 15 bitop3:0x78
	v_lshlrev_b32_e32 v34, 9, v6
	v_lshl_or_b32 v1, v1, 4, v34
	ds_read_b128 v[22:25], v1
	v_and_b32_e32 v1, 15, v0
	v_bitop3_b32 v26, v38, v1, 2 bitop3:0x36
	v_lshl_or_b32 v52, v26, 4, v34
	ds_read_b128 v[52:55], v52
	v_bitop3_b32 v56, v38, v1, 4 bitop3:0x36
	v_lshl_or_b32 v56, v56, 4, v34
	ds_read_b128 v[56:59], v56
	s_movk_i32 s0, 0x80
	v_cmp_gt_u32_e32 vcc, s0, v0
	s_waitcnt vmcnt(11) lgkmcnt(2)
	v_mfma_f32_32x32x16_f16 v[2:17], v[22:25], v[64:67], 0
	s_waitcnt vmcnt(10) lgkmcnt(1)
	v_mfma_f32_32x32x16_f16 v[2:17], v[52:55], v[68:71], v[2:17]
	s_waitcnt vmcnt(8)
	v_mfma_f32_32x32x16_f16 v[18:33], v[22:25], v[76:79], 0
	s_waitcnt vmcnt(7)
	v_mfma_f32_32x32x16_f16 v[18:33], v[52:55], v[80:83], v[18:33]
	v_bitop3_b32 v52, v38, v1, 6 bitop3:0x36
	v_lshl_or_b32 v34, v52, 4, v34
	s_waitcnt lgkmcnt(0)
	v_mfma_f32_32x32x16_f16 v[2:17], v[56:59], v[72:75], v[2:17]
	s_waitcnt vmcnt(6)
	v_mfma_f32_32x32x16_f16 v[18:33], v[56:59], v[84:87], v[18:33]
	ds_read_b128 v[40:43], v34
	v_mov_b32_e32 v34, v35
	s_waitcnt vmcnt(5) lgkmcnt(0)
	v_mfma_f32_32x32x16_f16 v[2:17], v[40:43], v[88:91], v[2:17]
	s_waitcnt vmcnt(4)
	v_mfma_f32_32x32x16_f16 v[18:33], v[40:43], v[92:95], v[18:33]
	s_waitcnt vmcnt(2)
	v_cndmask_b32_e32 v34, 0, v96, vcc
	v_cndmask_b32_e32 v35, 0, v97, vcc
	s_nop 7
	v_add_f32_e32 v2, v2, v34
	v_cvt_f16_f32_e32 v2, v2
	v_add_f32_e32 v18, v18, v35
	v_lshlrev_b32_e32 v37, 1, v37
	s_movk_i32 s0, 0xff80
	v_cvt_f16_f32_e32 v18, v18
	v_add_f32_e32 v3, v3, v34
	v_and_or_b32 v37, v0, s0, v37
	v_lshlrev_b32_e32 v38, 11, v38
	v_lshlrev_b32_e32 v39, 9, v39
	v_cvt_f16_f32_e32 v3, v3
	v_add_f32_e32 v19, v19, v35
	v_add3_u32 v37, v37, v38, v39
	v_cvt_f16_f32_e32 v19, v19
	ds_write_b16 v37, v2 offset:256
	ds_write_b16 v37, v18 offset:320
	ds_write_b16 v37, v3 offset:768
	ds_write_b16 v37, v19 offset:832
	v_add_f32_e32 v2, v4, v34
	v_cvt_f16_f32_e32 v2, v2
	v_add_f32_e32 v3, v20, v35
	v_cvt_f16_f32_e32 v3, v3
	v_add_f32_e32 v4, v5, v34
	v_cvt_f16_f32_e32 v4, v4
	v_add_f32_e32 v5, v21, v35
	v_cvt_f16_f32_e32 v5, v5
	ds_write_b16 v37, v2 offset:1280
	ds_write_b16 v37, v3 offset:1344
	ds_write_b16 v37, v4 offset:1792
	ds_write_b16 v37, v5 offset:1856
	v_add_f32_e32 v2, v6, v34
	v_cvt_f16_f32_e32 v2, v2
	v_add_f32_e32 v3, v22, v35
	v_cvt_f16_f32_e32 v3, v3
	v_add_f32_e32 v4, v7, v34
	v_cvt_f16_f32_e32 v4, v4
	v_add_f32_e32 v5, v23, v35
	v_cvt_f16_f32_e32 v5, v5
	ds_write_b16 v37, v2 offset:4352
	ds_write_b16 v37, v3 offset:4416
	ds_write_b16 v37, v4 offset:4864
	ds_write_b16 v37, v5 offset:4928
	v_add_f32_e32 v2, v8, v34
	v_cvt_f16_f32_e32 v2, v2
	v_add_f32_e32 v3, v24, v35
	v_cvt_f16_f32_e32 v3, v3
	v_add_f32_e32 v4, v9, v34
	v_cvt_f16_f32_e32 v4, v4
	v_add_f32_e32 v5, v25, v35
	v_cvt_f16_f32_e32 v5, v5
	ds_write_b16 v37, v2 offset:5376
	ds_write_b16 v37, v3 offset:5440
	ds_write_b16 v37, v4 offset:5888
	ds_write_b16 v37, v5 offset:5952
	v_add_f32_e32 v2, v10, v34
	v_cvt_f16_f32_e32 v2, v2
	v_add_f32_e32 v3, v26, v35
	v_cvt_f16_f32_e32 v3, v3
	v_add_f32_e32 v4, v11, v34
	v_cvt_f16_f32_e32 v4, v4
	v_add_f32_e32 v5, v27, v35
	v_cvt_f16_f32_e32 v5, v5
	ds_write_b16 v37, v2 offset:8448
	ds_write_b16 v37, v3 offset:8512
	ds_write_b16 v37, v4 offset:8960
	ds_write_b16 v37, v5 offset:9024
	v_add_f32_e32 v2, v12, v34
	v_cvt_f16_f32_e32 v2, v2
	v_add_f32_e32 v3, v28, v35
	v_cvt_f16_f32_e32 v3, v3
	v_add_f32_e32 v4, v13, v34
	v_cvt_f16_f32_e32 v4, v4
	v_add_f32_e32 v5, v29, v35
	v_cvt_f16_f32_e32 v5, v5
	ds_write_b16 v37, v2 offset:9472
	ds_write_b16 v37, v3 offset:9536
	ds_write_b16 v37, v4 offset:9984
	ds_write_b16 v37, v5 offset:10048
	v_add_f32_e32 v2, v14, v34
	v_cvt_f16_f32_e32 v2, v2
	v_add_f32_e32 v3, v30, v35
	v_cvt_f16_f32_e32 v3, v3
	v_add_f32_e32 v4, v15, v34
	v_cvt_f16_f32_e32 v4, v4
	v_add_f32_e32 v5, v31, v35
	v_cvt_f16_f32_e32 v5, v5
	ds_write_b16 v37, v2 offset:12544
	ds_write_b16 v37, v3 offset:12608
	ds_write_b16 v37, v4 offset:13056
	ds_write_b16 v37, v5 offset:13120
	v_add_f32_e32 v2, v16, v34
	v_cvt_f16_f32_e32 v2, v2
	v_add_f32_e32 v3, v32, v35
	v_cvt_f16_f32_e32 v3, v3
	v_add_f32_e32 v4, v17, v34
	v_cvt_f16_f32_e32 v4, v4
	v_add_f32_e32 v5, v33, v35
	v_cvt_f16_f32_e32 v5, v5
	s_mov_b64 s[4:5], -1
	v_ashrrev_i32_e32 v9, 4, v0
	s_mov_b64 s[0:1], 0
	s_and_b64 vcc, exec, 0
	ds_write_b16 v37, v2 offset:13568
	ds_write_b16 v37, v3 offset:13632
	ds_write_b16 v37, v4 offset:14080
	ds_write_b16 v37, v5 offset:14144
	s_waitcnt lgkmcnt(0)
	s_barrier
	s_cbranch_vccnz .LBB2_83
	v_lshlrev_b32_e32 v2, 2, v9
	ds_read_b32 v8, v2 offset:40448
	s_andn2_b64 vcc, exec, s[0:1]
	s_cbranch_vccnz .LBB2_68
